# MoBA loop: dropped unneeded MFMA-result nop pads and dead zero-inits before cvt_pk_fp8; first four V-fragment LDS reads of P.V issued early into free registers
# baseline (speedup 1.0000x reference)
; #define SBAR() __builtin_amdgcn_sched_barrier(0)
; __device__ __forceinline__ void finishSM8(f32x16& p0, f32x16& p1, float alpha, float& l_reg, i32x8& pa) {
;     for (int r = 0; r < 16; ++r) p1[r] = __builtin_amdgcn_exp2f(p1[r]);
;     float ps;
;     { float s0 = p0[0] + p0[1], s1 = p0[2] + p0[3], s2 = p1[0] + p1[1], s3 = p1[2] + p1[3];
; #pragma unroll
;       for (int r = 4; r < 16; r += 4) { s0 += p0[r]; s0 += p0[r + 1]; s1 += p0[r + 2]; s1 += p0[r + 3]; s2 += p1[r]; s2 += p1[r + 1]; s3 += p1[r + 2]; s3 += p1[r + 3]; }
;       ps = (s0 + s1) + (s2 + s3); }
;     { auto rr = __builtin_amdgcn_permlane32_swap(__float_as_uint(ps), __float_as_uint(ps), false, false);
;       ps = __uint_as_float(rr[0]) + __uint_as_float(rr[1]); }
;     l_reg = l_reg * alpha + ps;
; #pragma unroll
;     for (int d = 0; d < 4; ++d) { int w0 = 0, w1 = 0;
;         w0 = __builtin_amdgcn_cvt_pk_fp8_f32(p0[4 * d], p0[4 * d + 1], w0, false); w0 = __builtin_amdgcn_cvt_pk_fp8_f32(p0[4 * d + 2], p0[4 * d + 3], w0, true);
;         w1 = __builtin_amdgcn_cvt_pk_fp8_f32(p1[4 * d], p1[4 * d + 1], w1, false); w1 = __builtin_amdgcn_cvt_pk_fp8_f32(p1[4 * d + 2], p1[4 * d + 3], w1, true);
;         pa[d] = w0; pa[4 + d] = w1; }
; template <int KB, bool LOWREG = false>
; __device__ __forceinline__ void qkt_f8(f32x16& p0, f32x16& p1, const char* K_lds, int r32, int hi, const i32x8 (&q8)[2]) {
;     ...
;     i32x8 kf[2][2];
; #pragma unroll
;     for (int c = 0; c < 2; ++c) { const unsigned a0 = base + ((((unsigned)(4 * c + 2 * hi)) ^ sw) << 4), a1 = base + ((((unsigned)(4 * c + 2 * hi + 1)) ^ sw) << 4);
; #pragma unroll
;         for (int hf = 0; hf < 2; ++hf)
;             kf[c][hf] = __builtin_bit_cast(i32x8, __builtin_shufflevector(*(lds_f)(__UINTPTR_TYPE__)(a0 + hf * 4096), *(lds_f)(__UINTPTR_TYPE__)(a1 + hf * 4096), 0, 1, 2, 3, 4, 5, 6, 7, 8, 9, 10, 11, 12, 13, 14, 15)); }
;     SBAR();
;     asm volatile("v_mfma_f32_32x32x64_f8f6f4 %0, %1, %2, 0" : "=&v"(p0) : "v"(kf[0][0]), "v"(q8[0]));
;     asm volatile("v_mfma_f32_32x32x64_f8f6f4 %0, %1, %2, 0" : "=&v"(p1) : "v"(kf[0][1]), "v"(q8[0]));
;     asm volatile("v_mfma_f32_32x32x64_f8f6f4 %0, %1, %2, %0" : "+v"(p0) : "v"(kf[1][0]), "v"(q8[1]));
;     asm volatile("v_mfma_f32_32x32x64_f8f6f4 %0, %1, %2, %0" : "+v"(p1) : "v"(kf[1][1]), "v"(q8[1]));
;     asm volatile("s_nop 15\n\ts_nop 15" ::: "memory");
;     SBAR();
.LBB0_1043:
	v_mov_b32_e32 v2, v152
	v_mov_b32_e32 v4, v130
	s_cmp_lg_u32 s79, -1
	s_cselect_b32 s6, s79, 0
	v_lshrrev_b32_e32 v12, 1, v4
	s_addk_i32 s6, 0x4000
	v_lshlrev_b32_e32 v2, 1, v2
	v_bfe_u32 v5, v4, 1, 3
	v_lshl_add_u32 v13, v4, 7, s6
	v_bitop3_b32 v4, v12, v2, 7 bitop3:0x6c
	v_lshl_add_u32 v8, v4, 4, v13
	v_bitop3_b32 v4, v2, v5, 1 bitop3:0x36
	v_lshl_add_u32 v14, v4, 4, v13
	ds_read_b128 v[4:7], v8
	ds_read_b128 v[184:187], v8 offset:4096
	ds_read_b128 v[8:11], v14
	ds_read_b128 v[188:191], v14 offset:4096
	v_add_u32_e32 v14, 4, v2
	v_bitop3_b32 v14, v14, v12, 7 bitop3:0x78
	v_add_u32_e32 v2, 5, v2
	v_lshl_add_u32 v14, v14, 4, v13
	v_bitop3_b32 v2, v2, v12, 7 bitop3:0x78
	v_lshl_add_u32 v2, v2, 4, v13
	ds_read_b128 v[200:203], v14
	ds_read_b128 v[218:221], v14 offset:4096
	ds_read_b128 v[204:207], v2
	ds_read_b128 v[222:225], v2 offset:4096
	s_waitcnt lgkmcnt(5)
	v_mfma_f32_32x32x64_f8f6f4 v[98:113], v[4:11], v[114:121], 0
	s_waitcnt lgkmcnt(4)
	v_mfma_f32_32x32x64_f8f6f4 v[82:97], v[184:191], v[114:121], 0
	s_waitcnt lgkmcnt(1)
	v_mfma_f32_32x32x64_f8f6f4 v[98:113], v[200:207], v[122:129], v[98:113]
	s_waitcnt lgkmcnt(0)
	v_mfma_f32_32x32x64_f8f6f4 v[82:97], v[218:225], v[122:129], v[82:97]
	ds_read_b128 v[226:229], v157
	ds_read_b128 v[234:237], v157 offset:2048
	ds_read_b128 v[230:233], v158
	ds_read_b128 v[238:241], v158 offset:2048
	v_exp_f32_e32 v4, v148
	v_exp_f32_e32 v5, v149
	v_exp_f32_e32 v6, v144
	v_exp_f32_e32 v7, v145
	v_exp_f32_e32 v8, v142
	v_exp_f32_e32 v10, v138
	v_exp_f32_e32 v9, v143
	v_exp_f32_e32 v11, v139
	v_exp_f32_e32 v12, v136
	v_exp_f32_e32 v14, v150
	v_exp_f32_e32 v13, v137
	v_exp_f32_e32 v15, v151
	v_add_f32_e32 v2, v181, v182
	v_add_f32_e32 v136, v171, v173
	v_add_f32_e32 v137, v4, v5
	v_add_f32_e32 v138, v6, v7
	v_exp_f32_e32 v16, v146
	v_exp_f32_e32 v144, v140
	v_add_f32_e32 v2, v179, v2
	v_add_f32_e32 v136, v176, v136
	v_add_f32_e32 v137, v8, v137
	v_add_f32_e32 v138, v10, v138
	v_exp_f32_e32 v17, v147
	v_exp_f32_e32 v145, v141
	v_add_f32_e32 v2, v180, v2
	v_add_f32_e32 v136, v178, v136
	v_add_f32_e32 v137, v9, v137
	v_add_f32_e32 v138, v11, v138
	v_add_f32_e32 v2, v175, v2
	v_add_f32_e32 v136, v167, v136
	v_add_f32_e32 v137, v12, v137
	v_add_f32_e32 v138, v14, v138
	v_add_f32_e32 v2, v177, v2
	v_add_f32_e32 v136, v168, v136
	v_add_f32_e32 v137, v13, v137
	v_add_f32_e32 v138, v15, v138
	v_add_f32_e32 v2, v172, v2
	v_add_f32_e32 v136, v169, v136
	v_add_f32_e32 v137, v16, v137
	v_add_f32_e32 v138, v144, v138
	v_add_f32_e32 v2, v174, v2
	v_add_f32_e32 v136, v170, v136
	v_add_f32_e32 v137, v17, v137
	v_add_f32_e32 v138, v145, v138
	v_add_f32_e32 v2, v136, v2
	v_add_f32_e32 v136, v137, v138
	v_cvt_pk_fp8_f32 v142, v12, v13
	v_add_f32_e32 v2, v2, v136
	v_cvt_pk_fp8_f32 v136, v181, v182
	v_cvt_pk_fp8_f32 v140, v4, v5
	v_cvt_pk_fp8_f32 v137, v179, v180
	v_cvt_pk_fp8_f32 v141, v8, v9
	v_cvt_pk_fp8_f32 v138, v175, v177
	v_cvt_pk_fp8_f32 v139, v172, v174
	v_cvt_pk_fp8_f32 v143, v16, v17
	v_cvt_pk_fp8_f32 v142, v14, v15 op_sel:[0,0,1]
	v_mov_b32_e32 v14, v2
	s_nop 1
	v_permlane32_swap_b32_e32 v2, v14
	v_cvt_pk_fp8_f32 v136, v171, v173 op_sel:[0,0,1]
	v_cvt_pk_fp8_f32 v140, v6, v7 op_sel:[0,0,1]
	v_cvt_pk_fp8_f32 v137, v176, v178 op_sel:[0,0,1]
	v_cvt_pk_fp8_f32 v141, v10, v11 op_sel:[0,0,1]
	v_cvt_pk_fp8_f32 v138, v167, v168 op_sel:[0,0,1]
	v_cvt_pk_fp8_f32 v139, v169, v170 op_sel:[0,0,1]
	v_cvt_pk_fp8_f32 v143, v144, v145 op_sel:[0,0,1]
	v_add_u32_e32 v12, s90, v165
	v_subrev_u32_e32 v6, 64, v12
	s_sub_i32 s86, s90, 64
	v_ashrrev_i32_e32 v7, 31, v6
	s_lshl_b64 s[6:7], s[86:87], 7
	v_lshlrev_b64 v[6:7], 7, v[6:7]
	v_lshl_add_u64 v[4:5], v[132:133], 0, s[6:7]
	v_lshl_add_u64 v[8:9], v[134:135], 0, v[6:7]
	global_load_dwordx4 v[4:7], v[4:5], off
	s_nop 0
	global_load_dwordx4 v[8:11], v[8:9], off
	ds_read_b128 v[144:147], v157 offset:4096
	ds_read_b128 v[148:151], v158 offset:4096
	ds_read_b128 v[166:169], v157 offset:6144
	ds_read_b128 v[170:173], v158 offset:6144
	s_waitcnt lgkmcnt(4)
	v_mfma_f32_32x32x64_f8f6f4 v[34:49], v[136:143], v[226:233], v[34:49]
	v_mfma_f32_32x32x64_f8f6f4 v[50:65], v[136:143], v[234:241], v[50:65]
	s_waitcnt lgkmcnt(2)
	v_mfma_f32_32x32x64_f8f6f4 v[18:33], v[136:143], v[144:151], v[18:33]
	s_waitcnt lgkmcnt(0)
	v_mfma_f32_32x32x64_f8f6f4 v[66:81], v[136:143], v[166:173], v[66:81]
	s_add_i32 s6, s90, 0xffffffbf
	s_cmp_le_i32 s6, s78
	s_cbranch_scc1 .LBB0_1045
; __device__ __forceinline__ void mask_tile_perm(f32x16& p0, f32x16& p1, int dq) {
;     const float NEG = -__builtin_inff();
; #pragma unroll
;     for (int r = 0; r < 16; ++r) { const int c = 16 * (r & 3) + (r >> 2);
;         if (dq - c < 0) p0[r] = NEG;
;         if (dq - c - 4 < 0) p1[r] = NEG; }
; }
	v_add_u32_e32 v13, 64, v164
	v_cmp_gt_i32_e64 s[58:59], 50, v13
	v_cmp_gt_i32_e64 s[66:67], 51, v13
	v_cmp_gt_i32_e64 s[50:51], 49, v13
	s_and_b64 s[58:59], s[66:67], s[58:59]
	v_cmp_gt_i32_e64 s[42:43], 48, v13
	s_and_b64 s[50:51], s[58:59], s[50:51]
	v_cmp_gt_i32_e64 s[40:41], 32, v13
	s_and_b64 s[42:43], s[50:51], s[42:43]
	v_cmp_gt_i32_e64 s[38:39], 16, v13
	s_and_b64 s[40:41], s[42:43], s[40:41]
	v_cmp_gt_i32_e64 s[36:37], 0, v13
	s_and_b64 s[38:39], s[40:41], s[38:39]
	s_and_b64 s[36:37], s[38:39], s[36:37]
	v_cmp_gt_i32_e64 s[28:29], 54, v13
	v_cndmask_b32_e64 v98, v98, v210, s[36:37]
	v_cmp_gt_i32_e64 s[36:37], 55, v13
	v_cmp_gt_i32_e64 s[20:21], 53, v13
	s_and_b64 s[28:29], s[36:37], s[28:29]
	v_cmp_gt_i32_e64 s[12:13], 52, v13
	s_and_b64 s[20:21], s[28:29], s[20:21]
	v_cmp_gt_i32_e64 s[8:9], 36, v13
	v_cmp_gt_i32_e64 s[48:49], 33, v13
	v_cmp_gt_i32_e64 s[16:17], 37, v13
	v_cmp_gt_i32_e64 s[56:57], 34, v13
	v_cmp_gt_i32_e64 s[24:25], 38, v13
	v_cmp_gt_i32_e64 s[64:65], 35, v13
	v_cmp_gt_i32_e64 s[34:35], 39, v13
	s_and_b64 s[12:13], s[20:21], s[12:13]
	v_cmp_gt_i32_e64 s[6:7], 20, v13
	v_cmp_gt_i32_e64 s[46:47], 17, v13
	v_cmp_gt_i32_e64 s[14:15], 21, v13
	v_cmp_gt_i32_e64 s[54:55], 18, v13
	v_cmp_gt_i32_e64 s[22:23], 22, v13
	v_cmp_gt_i32_e64 s[62:63], 19, v13
	v_cmp_gt_i32_e64 s[30:31], 23, v13
	s_and_b64 s[64:65], s[66:67], s[64:65]
	s_and_b64 s[56:57], s[58:59], s[56:57]
	s_and_b64 s[48:49], s[50:51], s[48:49]
	s_and_b64 s[34:35], s[36:37], s[34:35]
	s_and_b64 s[24:25], s[28:29], s[24:25]
	s_and_b64 s[16:17], s[20:21], s[16:17]
	s_and_b64 s[8:9], s[12:13], s[8:9]
	v_cmp_gt_i32_e32 vcc, 4, v13
	v_cmp_gt_i32_e64 s[44:45], 1, v13
	v_cmp_gt_i32_e64 s[10:11], 5, v13
	v_cmp_gt_i32_e64 s[52:53], 2, v13
	v_cmp_gt_i32_e64 s[18:19], 6, v13
	v_cmp_gt_i32_e64 s[60:61], 3, v13
	v_cmp_gt_i32_e64 s[26:27], 7, v13
	s_and_b64 s[62:63], s[64:65], s[62:63]
	s_and_b64 s[54:55], s[56:57], s[54:55]
	s_and_b64 s[46:47], s[48:49], s[46:47]
	s_and_b64 s[30:31], s[34:35], s[30:31]
	s_and_b64 s[22:23], s[24:25], s[22:23]
	s_and_b64 s[14:15], s[16:17], s[14:15]
	s_and_b64 s[6:7], s[8:9], s[6:7]
	v_cndmask_b32_e64 v109, v109, v210, s[58:59]
	v_cndmask_b32_e64 v105, v105, v210, s[50:51]
	s_and_b64 s[58:59], s[62:63], s[60:61]
	v_cndmask_b32_e64 v101, v101, v210, s[42:43]
	s_and_b64 s[50:51], s[54:55], s[52:53]
	s_and_b64 s[42:43], s[46:47], s[44:45]
	s_and_b64 s[26:27], s[30:31], s[26:27]
	s_and_b64 s[18:19], s[22:23], s[18:19]
	s_and_b64 s[10:11], s[14:15], s[10:11]
	s_and_b64 vcc, s[6:7], vcc
	v_cndmask_b32_e64 v113, v113, v210, s[66:67]
	v_cndmask_b32_e64 v112, v112, v210, s[64:65]
	v_cndmask_b32_e64 v111, v111, v210, s[62:63]
	v_cndmask_b32_e64 v108, v108, v210, s[56:57]
	v_cndmask_b32_e64 v110, v110, v210, s[58:59]
	v_cndmask_b32_e64 v107, v107, v210, s[54:55]
	v_cndmask_b32_e64 v104, v104, v210, s[48:49]
	v_cndmask_b32_e64 v106, v106, v210, s[50:51]
	v_cndmask_b32_e64 v103, v103, v210, s[46:47]
	v_cndmask_b32_e64 v100, v100, v210, s[40:41]
	v_cndmask_b32_e64 v102, v102, v210, s[42:43]
	v_cndmask_b32_e64 v99, v99, v210, s[38:39]
	v_cndmask_b32_e64 v97, v97, v210, s[36:37]
	v_cndmask_b32_e64 v96, v96, v210, s[34:35]
	v_cndmask_b32_e64 v93, v93, v210, s[28:29]
	v_cndmask_b32_e64 v95, v95, v210, s[30:31]
	v_cndmask_b32_e64 v92, v92, v210, s[24:25]
	v_cndmask_b32_e64 v89, v89, v210, s[20:21]
	v_cndmask_b32_e64 v94, v94, v210, s[26:27]
	v_cndmask_b32_e64 v91, v91, v210, s[22:23]
	v_cndmask_b32_e64 v88, v88, v210, s[16:17]
	v_cndmask_b32_e64 v85, v85, v210, s[12:13]
	v_cndmask_b32_e64 v90, v90, v210, s[18:19]
	v_cndmask_b32_e64 v87, v87, v210, s[14:15]
	v_cndmask_b32_e64 v84, v84, v210, s[8:9]
	v_cndmask_b32_e64 v86, v86, v210, s[10:11]
	v_cndmask_b32_e64 v83, v83, v210, s[6:7]
	v_cndmask_b32_e32 v82, v82, v210, vcc

; #define SBAR() __builtin_amdgcn_sched_barrier(0)
;     ...
;     constexpr float SCL = SCALE / (float)(1 << SH), C2 = 1.4426950408889634f * SCL;
;     if (__builtin_expect(__all((pmax - m_reg) * SCL <= (float)THRI), 1)) { mn = m_reg; alpha = 1.f; }
;     else { mn = fmaxf(m_reg, pmax); alpha = __builtin_amdgcn_exp2f((m_reg - mn) * C2); m_reg = mn; }
;     const float mnL = dead ? -__builtin_inff() : -mn * C2 + (float)PSH;
;     for (int r = 0; r < 16; ++r) p0[r] = fmaf(p0[r], C2, mnL); for (int r = 0; r < 16; ++r) p1[r] = fmaf(p1[r], C2, mnL);
;     for (int r = 0; r < 16; ++r) p0[r] = __builtin_amdgcn_exp2f(p0[r]);
; template <int KB, bool LOWREG = false>
; __device__ __forceinline__ void qkt_f8(f32x16& p0, f32x16& p1, const char* K_lds, int r32, int hi, const i32x8 (&q8)[2]) {
;     ...
;     i32x8 kf[2][2];
; #pragma unroll
;     for (int c = 0; c < 2; ++c) { const unsigned a0 = base + ((((unsigned)(4 * c + 2 * hi)) ^ sw) << 4), a1 = base + ((((unsigned)(4 * c + 2 * hi + 1)) ^ sw) << 4);
; #pragma unroll
;         for (int hf = 0; hf < 2; ++hf)
;             kf[c][hf] = __builtin_bit_cast(i32x8, __builtin_shufflevector(*(lds_f)(__UINTPTR_TYPE__)(a0 + hf * 4096), *(lds_f)(__UINTPTR_TYPE__)(a1 + hf * 4096), 0, 1, 2, 3, 4, 5, 6, 7, 8, 9, 10, 11, 12, 13, 14, 15)); }
;     SBAR();
;     asm volatile("v_mfma_f32_32x32x64_f8f6f4 %0, %1, %2, 0" : "=&v"(p0) : "v"(kf[0][0]), "v"(q8[0]));
;     asm volatile("v_mfma_f32_32x32x64_f8f6f4 %0, %1, %2, 0" : "=&v"(p1) : "v"(kf[0][1]), "v"(q8[0]));
;     asm volatile("v_mfma_f32_32x32x64_f8f6f4 %0, %1, %2, %0" : "+v"(p0) : "v"(kf[1][0]), "v"(q8[1]));
;     asm volatile("v_mfma_f32_32x32x64_f8f6f4 %0, %1, %2, %0" : "+v"(p1) : "v"(kf[1][1]), "v"(q8[1]));
;     asm volatile("s_nop 15\n\ts_nop 15" ::: "memory");
;     SBAR();
.LBB0_1049:
	v_cndmask_b32_e64 v16, v13, v163, s[8:9]
	v_fmamk_f32 v13, v16, 0xba0293ee, v1
	v_cndmask_b32_e64 v13, v13, v210, s[6:7]
	v_fmamk_f32 v98, v98, 0x3a0293ee, v13
	v_fmamk_f32 v99, v99, 0x3a0293ee, v13
	v_fmamk_f32 v100, v100, 0x3a0293ee, v13
	v_fmamk_f32 v101, v101, 0x3a0293ee, v13
	v_fmamk_f32 v102, v102, 0x3a0293ee, v13
	v_fmamk_f32 v103, v103, 0x3a0293ee, v13
	v_fmamk_f32 v104, v104, 0x3a0293ee, v13
	v_fmamk_f32 v105, v105, 0x3a0293ee, v13
	v_fmamk_f32 v106, v106, 0x3a0293ee, v13
	v_fmamk_f32 v107, v107, 0x3a0293ee, v13
	v_fmamk_f32 v108, v108, 0x3a0293ee, v13
	v_fmamk_f32 v109, v109, 0x3a0293ee, v13
	v_fmamk_f32 v110, v110, 0x3a0293ee, v13
	v_fmamk_f32 v111, v111, 0x3a0293ee, v13
	v_fmamk_f32 v112, v112, 0x3a0293ee, v13
	v_fmamk_f32 v113, v113, 0x3a0293ee, v13
	v_exp_f32_e32 v150, v98
	v_exp_f32_e32 v151, v99
	v_exp_f32_e32 v142, v100
	v_exp_f32_e32 v144, v101
	v_exp_f32_e32 v148, v102
	v_exp_f32_e32 v149, v103
	v_exp_f32_e32 v146, v104
	v_exp_f32_e32 v147, v105
	v_exp_f32_e32 v143, v106
	v_exp_f32_e32 v145, v107
	v_exp_f32_e32 v136, v108
	v_exp_f32_e32 v137, v109
	v_exp_f32_e32 v140, v110
	v_exp_f32_e32 v141, v111
	v_exp_f32_e32 v138, v112
	v_exp_f32_e32 v139, v113
	v_fmamk_f32 v17, v82, 0x3a0293ee, v13
	v_fmamk_f32 v163, v83, 0x3a0293ee, v13
	v_fmamk_f32 v166, v84, 0x3a0293ee, v13
	v_fmamk_f32 v167, v85, 0x3a0293ee, v13
	v_fmamk_f32 v168, v86, 0x3a0293ee, v13
	v_fmamk_f32 v169, v87, 0x3a0293ee, v13
	v_fmamk_f32 v170, v88, 0x3a0293ee, v13
	v_fmamk_f32 v171, v89, 0x3a0293ee, v13
	v_fmamk_f32 v172, v90, 0x3a0293ee, v13
	v_fmamk_f32 v173, v91, 0x3a0293ee, v13
	v_fmamk_f32 v174, v92, 0x3a0293ee, v13
	v_fmamk_f32 v175, v93, 0x3a0293ee, v13
	v_fmamk_f32 v176, v94, 0x3a0293ee, v13
	v_fmamk_f32 v177, v95, 0x3a0293ee, v13
	v_fmamk_f32 v178, v96, 0x3a0293ee, v13
	v_fmac_f32_e32 v13, 0x3a0293ee, v97
	s_waitcnt lgkmcnt(0)
	s_barrier
	v_mov_b32_e32 v82, v130
	v_mov_b32_e32 v83, v152
	s_cmp_lg_u32 s79, -1
	s_cselect_b32 s6, s79, 0
	v_lshrrev_b32_e32 v90, 1, v82
	v_lshlrev_b32_e32 v92, 1, v83
	v_bfe_u32 v84, v82, 1, 3
	v_lshl_add_u32 v91, v82, 7, s6
	v_bitop3_b32 v82, v90, v92, 7 bitop3:0x6c
	v_lshl_add_u32 v86, v82, 4, v91
	v_bitop3_b32 v82, v92, v84, 1 bitop3:0x36
	v_lshl_add_u32 v93, v82, 4, v91
	ds_read_b128 v[82:85], v86
	ds_read_b128 v[180:183], v86 offset:4096
	ds_read_b128 v[86:89], v93
	ds_read_b128 v[184:187], v93 offset:4096
	v_add_u32_e32 v93, 4, v92
	v_bitop3_b32 v93, v93, v90, 7 bitop3:0x78
	v_add_u32_e32 v92, 5, v92
	v_lshl_add_u32 v93, v93, 4, v91
	v_bitop3_b32 v90, v92, v90, 7 bitop3:0x78
	v_lshl_add_u32 v90, v90, 4, v91
	ds_read_b128 v[188:191], v93
	ds_read_b128 v[200:203], v93 offset:4096
	ds_read_b128 v[192:195], v90
	ds_read_b128 v[204:207], v90 offset:4096
	s_waitcnt lgkmcnt(5)
	v_mfma_f32_32x32x64_f8f6f4 v[98:113], v[82:89], v[114:121], 0
	s_waitcnt lgkmcnt(4)
	v_mfma_f32_32x32x64_f8f6f4 v[82:97], v[180:187], v[114:121], 0
	s_waitcnt lgkmcnt(1)
	v_mfma_f32_32x32x64_f8f6f4 v[98:113], v[188:195], v[122:129], v[98:113]
	s_waitcnt lgkmcnt(0)
	v_mfma_f32_32x32x64_f8f6f4 v[82:97], v[200:207], v[122:129], v[82:97]
	ds_read_b128 v[226:229], v157 offset:16384
	ds_read_b128 v[234:237], v157 offset:18432
	ds_read_b128 v[230:233], v158 offset:16384
	ds_read_b128 v[238:241], v158 offset:18432
	v_exp_f32_e32 v185, v17
	v_exp_f32_e32 v186, v163
	v_exp_f32_e32 v179, v166
	v_exp_f32_e32 v180, v167
	v_exp_f32_e32 v183, v168
	v_exp_f32_e32 v181, v170
	v_exp_f32_e32 v184, v169
	v_exp_f32_e32 v182, v171
	v_exp_f32_e32 v172, v172
	v_exp_f32_e32 v163, v174
	v_exp_f32_e32 v173, v173
	v_exp_f32_e32 v167, v175
	v_exp_f32_e32 v169, v13
	v_add_f32_e32 v13, v150, v151
	v_add_f32_e32 v17, v142, v144
	v_add_f32_e32 v166, v185, v186
	v_add_f32_e32 v174, v179, v180
	v_exp_f32_e32 v170, v176
	v_exp_f32_e32 v168, v178
	v_add_f32_e32 v13, v148, v13
	v_add_f32_e32 v17, v146, v17
	v_add_f32_e32 v166, v183, v166
	v_add_f32_e32 v174, v181, v174
	v_exp_f32_e32 v171, v177
	v_add_f32_e32 v13, v149, v13
	v_add_f32_e32 v17, v147, v17
	v_add_f32_e32 v166, v184, v166
	v_add_f32_e32 v174, v182, v174
	v_add_f32_e32 v13, v143, v13
	v_add_f32_e32 v17, v136, v17
	v_add_f32_e32 v166, v172, v166
	v_add_f32_e32 v174, v163, v174
	v_add_f32_e32 v13, v145, v13
	v_add_f32_e32 v17, v137, v17
	v_add_f32_e32 v166, v173, v166
	v_add_f32_e32 v174, v167, v174
	v_add_f32_e32 v13, v140, v13
	v_add_f32_e32 v17, v138, v17
	v_add_f32_e32 v166, v170, v166
	v_add_f32_e32 v174, v168, v174
	v_add_f32_e32 v13, v141, v13
	v_add_f32_e32 v17, v139, v17
	v_add_f32_e32 v166, v171, v166
	v_add_f32_e32 v174, v169, v174
	v_add_f32_e32 v13, v17, v13
	v_add_f32_e32 v17, v166, v174
	v_add_f32_e32 v17, v17, v13
	v_mov_b32_e32 v166, v17
	s_nop 1
	v_permlane32_swap_b32_e32 v17, v166
	s_add_i32 s6, s81, 1
	s_cmp_lt_u32 s6, s80
	s_cselect_b64 s[70:71], -1, 0
	s_cmp_ge_u32 s6, s80
	s_cbranch_scc1 .LBB0_1051
	v_ashrrev_i32_e32 v13, 31, v12
	s_mov_b32 s91, s87
	v_lshlrev_b64 v[4:5], 7, v[12:13]
	s_lshl_b64 s[6:7], s[90:91], 7
	v_lshl_add_u64 v[8:9], v[134:135], 0, v[4:5]
	v_lshl_add_u64 v[4:5], v[132:133], 0, s[6:7]
	global_load_dwordx4 v[4:7], v[4:5], off
	s_nop 0
	global_load_dwordx4 v[8:11], v[8:9], off
; __device__ __forceinline__ void finishSM8(f32x16& p0, f32x16& p1, float alpha, float& l_reg, i32x8& pa) {
;     ...
;     for (int d = 0; d < 4; ++d) { int w0 = 0, w1 = 0;
;         w0 = __builtin_amdgcn_cvt_pk_fp8_f32(p0[4 * d], p0[4 * d + 1], w0, false); w0 = __builtin_amdgcn_cvt_pk_fp8_f32(p0[4 * d + 2], p0[4 * d + 3], w0, true);
;         w1 = __builtin_amdgcn_cvt_pk_fp8_f32(p1[4 * d], p1[4 * d + 1], w1, false); w1 = __builtin_amdgcn_cvt_pk_fp8_f32(p1[4 * d + 2], p1[4 * d + 3], w1, true);
;         pa[d] = w0; pa[4 + d] = w1; }
; __device__ __forceinline__ void mask_tile_perm(f32x16& p0, f32x16& p1, int dq) {
;     const float NEG = -__builtin_inff();
; #pragma unroll
;     for (int r = 0; r < 16; ++r) { const int c = 16 * (r & 3) + (r >> 2);
;         if (dq - c < 0) p0[r] = NEG;
;         if (dq - c - 4 < 0) p1[r] = NEG; }
; }
.LBB0_1051:
	v_cvt_pk_fp8_f32 v188, v150, v151
	v_cvt_pk_fp8_f32 v192, v185, v186
	v_cvt_pk_fp8_f32 v189, v148, v149
	v_cvt_pk_fp8_f32 v193, v183, v184
	v_cvt_pk_fp8_f32 v190, v143, v145
	v_cvt_pk_fp8_f32 v194, v172, v173
	v_cvt_pk_fp8_f32 v191, v140, v141
	v_cvt_pk_fp8_f32 v195, v170, v171
	v_cvt_pk_fp8_f32 v188, v142, v144 op_sel:[0,0,1]
	v_cvt_pk_fp8_f32 v192, v179, v180 op_sel:[0,0,1]
	v_cvt_pk_fp8_f32 v189, v146, v147 op_sel:[0,0,1]
	v_cvt_pk_fp8_f32 v193, v181, v182 op_sel:[0,0,1]
	v_cvt_pk_fp8_f32 v190, v136, v137 op_sel:[0,0,1]
	v_cvt_pk_fp8_f32 v194, v163, v167 op_sel:[0,0,1]
	v_cvt_pk_fp8_f32 v191, v138, v139 op_sel:[0,0,1]
	v_cvt_pk_fp8_f32 v195, v168, v169 op_sel:[0,0,1]
	ds_read_b128 v[136:139], v157 offset:20480
	ds_read_b128 v[140:143], v158 offset:20480
	ds_read_b128 v[144:147], v157 offset:22528
	ds_read_b128 v[148:151], v158 offset:22528
	s_waitcnt lgkmcnt(4)
	v_mfma_f32_32x32x64_f8f6f4 v[34:49], v[188:195], v[226:233], v[34:49]
	v_mfma_f32_32x32x64_f8f6f4 v[50:65], v[188:195], v[234:241], v[50:65]
	s_waitcnt lgkmcnt(2)
	v_mfma_f32_32x32x64_f8f6f4 v[18:33], v[188:195], v[136:143], v[18:33]
	s_waitcnt lgkmcnt(0)
	v_mfma_f32_32x32x64_f8f6f4 v[66:81], v[188:195], v[144:151], v[66:81]
	s_add_i32 s6, s90, -1
	s_cmp_le_i32 s6, s78
	s_cbranch_scc1 .LBB0_1053
	v_cmp_gt_i32_e64 s[58:59], 50, v164
	v_cmp_gt_i32_e64 s[66:67], 51, v164
	v_cmp_gt_i32_e64 s[50:51], 49, v164
	s_and_b64 s[58:59], s[66:67], s[58:59]
	v_cmp_gt_i32_e64 s[42:43], 48, v164
	s_and_b64 s[50:51], s[58:59], s[50:51]
	v_cmp_gt_i32_e64 s[40:41], 32, v164
	s_and_b64 s[42:43], s[50:51], s[42:43]
	v_cmp_gt_i32_e64 s[38:39], 16, v164
	s_and_b64 s[40:41], s[42:43], s[40:41]
	v_cmp_gt_i32_e64 s[36:37], 0, v164
	s_and_b64 s[38:39], s[40:41], s[38:39]
	s_and_b64 s[36:37], s[38:39], s[36:37]
	v_cmp_gt_i32_e64 s[28:29], 54, v164
	v_cndmask_b32_e64 v98, v98, v210, s[36:37]
	v_cmp_gt_i32_e64 s[36:37], 55, v164
	v_cmp_gt_i32_e64 s[20:21], 53, v164
	s_and_b64 s[28:29], s[36:37], s[28:29]
	v_cmp_gt_i32_e64 s[12:13], 52, v164
	s_and_b64 s[20:21], s[28:29], s[20:21]
	v_cmp_gt_i32_e64 s[8:9], 36, v164
	v_cmp_gt_i32_e64 s[48:49], 33, v164
	v_cmp_gt_i32_e64 s[16:17], 37, v164
	v_cmp_gt_i32_e64 s[56:57], 34, v164
	v_cmp_gt_i32_e64 s[24:25], 38, v164
	v_cmp_gt_i32_e64 s[64:65], 35, v164
	v_cmp_gt_i32_e64 s[34:35], 39, v164
	s_and_b64 s[12:13], s[20:21], s[12:13]
	v_cmp_gt_i32_e64 s[6:7], 20, v164
	v_cmp_gt_i32_e64 s[46:47], 17, v164
	v_cmp_gt_i32_e64 s[14:15], 21, v164
	v_cmp_gt_i32_e64 s[54:55], 18, v164
	v_cmp_gt_i32_e64 s[22:23], 22, v164
	v_cmp_gt_i32_e64 s[62:63], 19, v164
	v_cmp_gt_i32_e64 s[30:31], 23, v164
	s_and_b64 s[64:65], s[66:67], s[64:65]
	s_and_b64 s[56:57], s[58:59], s[56:57]
	s_and_b64 s[48:49], s[50:51], s[48:49]
	s_and_b64 s[34:35], s[36:37], s[34:35]
	s_and_b64 s[24:25], s[28:29], s[24:25]
	s_and_b64 s[16:17], s[20:21], s[16:17]
	s_and_b64 s[8:9], s[12:13], s[8:9]
	v_cmp_gt_i32_e32 vcc, 4, v164
	v_cmp_gt_i32_e64 s[44:45], 1, v164
	v_cmp_gt_i32_e64 s[10:11], 5, v164
	v_cmp_gt_i32_e64 s[52:53], 2, v164
	v_cmp_gt_i32_e64 s[18:19], 6, v164
	v_cmp_gt_i32_e64 s[60:61], 3, v164
	v_cmp_gt_i32_e64 s[26:27], 7, v164
	s_and_b64 s[62:63], s[64:65], s[62:63]
	s_and_b64 s[54:55], s[56:57], s[54:55]
	s_and_b64 s[46:47], s[48:49], s[46:47]
	s_and_b64 s[30:31], s[34:35], s[30:31]
	s_and_b64 s[22:23], s[24:25], s[22:23]
	s_and_b64 s[14:15], s[16:17], s[14:15]
	s_and_b64 s[6:7], s[8:9], s[6:7]
	v_cndmask_b32_e64 v109, v109, v210, s[58:59]
	v_cndmask_b32_e64 v105, v105, v210, s[50:51]
	s_and_b64 s[58:59], s[62:63], s[60:61]
	v_cndmask_b32_e64 v101, v101, v210, s[42:43]
	s_and_b64 s[50:51], s[54:55], s[52:53]
	s_and_b64 s[42:43], s[46:47], s[44:45]
	s_and_b64 s[26:27], s[30:31], s[26:27]
	s_and_b64 s[18:19], s[22:23], s[18:19]
	s_and_b64 s[10:11], s[14:15], s[10:11]
	s_and_b64 vcc, s[6:7], vcc
	v_cndmask_b32_e64 v113, v113, v210, s[66:67]
	v_cndmask_b32_e64 v112, v112, v210, s[64:65]
	v_cndmask_b32_e64 v111, v111, v210, s[62:63]
	v_cndmask_b32_e64 v108, v108, v210, s[56:57]
	v_cndmask_b32_e64 v110, v110, v210, s[58:59]
	v_cndmask_b32_e64 v107, v107, v210, s[54:55]
	v_cndmask_b32_e64 v104, v104, v210, s[48:49]
	v_cndmask_b32_e64 v106, v106, v210, s[50:51]
	v_cndmask_b32_e64 v103, v103, v210, s[46:47]
	v_cndmask_b32_e64 v100, v100, v210, s[40:41]
	v_cndmask_b32_e64 v102, v102, v210, s[42:43]
	v_cndmask_b32_e64 v99, v99, v210, s[38:39]
	v_cndmask_b32_e64 v97, v97, v210, s[36:37]
	v_cndmask_b32_e64 v96, v96, v210, s[34:35]
	v_cndmask_b32_e64 v93, v93, v210, s[28:29]
	v_cndmask_b32_e64 v95, v95, v210, s[30:31]
	v_cndmask_b32_e64 v92, v92, v210, s[24:25]
	v_cndmask_b32_e64 v89, v89, v210, s[20:21]
	v_cndmask_b32_e64 v94, v94, v210, s[26:27]
	v_cndmask_b32_e64 v91, v91, v210, s[22:23]
	v_cndmask_b32_e64 v88, v88, v210, s[16:17]
	v_cndmask_b32_e64 v85, v85, v210, s[12:13]
	v_cndmask_b32_e64 v90, v90, v210, s[18:19]
	v_cndmask_b32_e64 v87, v87, v210, s[14:15]
	v_cndmask_b32_e64 v84, v84, v210, s[8:9]
	v_cndmask_b32_e64 v86, v86, v210, s[10:11]
	v_cndmask_b32_e64 v83, v83, v210, s[6:7]
	v_cndmask_b32_e32 v82, v82, v210, vcc
